# speedup vs baseline: 1.0052x; 1.0052x over previous
.Lprio_done:
	s_cmp_eq_u32 s3, 3
	v_lshl_add_u32 v0, s3, 17, v217
	v_add_u32_e32 v1, 0x20000, v0
	s_cselect_b64 vcc, -1, 0
	v_cndmask_b32_e32 v0, v1, v0, vcc
	v_or_b32_e32 v0, v0, v215
	v_ashrrev_i32_e32 v1, 31, v0
	v_lshl_add_u64 v[0:1], v[0:1], 2, s[40:41]
	v_mov_b32_e32 v2, v219
	v_mov_b32_e32 v3, v218
	global_load_dword v218, v[0:1], off
	global_load_dword v219, v[0:1], off offset:256
	v_add_f32_e32 v0, v2, v3
	s_nop 1
	v_add_f32_dpp v0, v0, v0 quad_perm:[1,0,3,2] row_mask:0xf bank_mask:0xf bound_ctrl:1
	s_nop 1
	v_add_f32_dpp v0, v0, v0 quad_perm:[2,3,0,1] row_mask:0xf bank_mask:0xf bound_ctrl:1
	s_nop 1
	v_add_f32_dpp v0, v0, v0 row_half_mirror row_mask:0xf bank_mask:0xf bound_ctrl:1
	s_nop 1
	v_add_f32_dpp v0, v0, v0 row_mirror row_mask:0xf bank_mask:0xf bound_ctrl:1
	s_nop 0
	v_readlane_b32 s1, v0, 16
	v_readlane_b32 s9, v0, 48
	v_readlane_b32 s0, v0, 0
	v_readlane_b32 s8, v0, 32
	v_mov_b32_e32 v0, s1
	v_mov_b32_e32 v1, s9
	v_add_f32_e32 v0, s0, v0
	v_add_f32_e32 v1, s8, v1
	v_add_f32_e32 v0, v0, v1
	v_fma_mixlo_f16 v1, v0, s33, v3
	v_fma_mixlo_f16 v0, v0, s33, v2
	ds_write_b16 v220, v1 offset:14
	ds_write_b16 v220, v0 offset:142
	ds_write_b16 v220, v1 offset:300
	ds_write_b16 v220, v0 offset:428
	ds_read2_b32 v[2:3], v223 offset0:2 offset1:3
	ds_read2_b32 v[0:1], v223 offset1:1
	ds_read2_b32 v[4:5], v223 offset0:32 offset1:33
	ds_read2_b32 v[6:7], v223 offset0:34 offset1:35
	s_mov_b32 s8, 0
	s_mov_b32 s9, s8
	s_mov_b32 s10, s8
	s_waitcnt lgkmcnt(3)
	v_or_b32_sdwa v8, v3, s34 dst_sel:DWORD dst_unused:UNUSED_PAD src0_sel:WORD_0 src1_sel:DWORD
	v_cndmask_b32_e64 v3, v8, v3, s[4:5]
	s_mov_b32 s11, s8
	s_mov_b32 s12, s8
	s_waitcnt lgkmcnt(2)
	v_mfma_f32_32x32x16_f16 v[64:79], v[200:203], v[0:3], 0
	ds_read2_b32 v[2:3], v224 offset0:2 offset1:3
	ds_read2_b32 v[0:1], v224 offset1:1
	ds_read2_b32 v[16:17], v225 offset1:1
	ds_read2_b32 v[18:19], v225 offset0:2 offset1:3
	s_mov_b32 s13, s8
	s_mov_b32 s14, s8
	s_mov_b32 s15, s8
	s_waitcnt lgkmcnt(3)
	v_or_b32_sdwa v8, v3, s34 dst_sel:DWORD dst_unused:UNUSED_PAD src0_sel:WORD_0 src1_sel:DWORD
	s_waitcnt lgkmcnt(0)
	v_or_b32_sdwa v20, v19, s34 dst_sel:DWORD dst_unused:UNUSED_PAD src0_sel:WORD_0 src1_sel:DWORD
	v_cndmask_b32_e64 v19, v20, v19, s[4:5]
	v_cndmask_b32_e64 v3, v8, v3, s[4:5]
	s_mov_b32 s16, s8
	v_mfma_f32_32x32x16_f16 v[16:31], v[200:203], v[16:19], 0
	s_mov_b32 s17, s8
	s_mov_b32 s18, s8
	s_mov_b32 s19, s8
	s_mov_b32 s20, s8
	s_mov_b32 s21, s8
	s_mov_b32 s22, s8
	s_mov_b32 s23, s8
	v_mfma_f32_32x32x16_f16 v[48:63], v[200:203], v[0:3], 0
	v_or_b32_sdwa v0, v7, s34 dst_sel:DWORD dst_unused:UNUSED_PAD src0_sel:WORD_0 src1_sel:DWORD
	v_cndmask_b32_e64 v7, v0, v7, s[4:5]
	s_nop 1
	v_mfma_f32_32x32x16_f16 v[32:47], v[200:203], v[4:7], 0
	v_mov_b64_e32 v[0:1], s[8:9]
	v_mov_b64_e32 v[2:3], s[10:11]
	v_mov_b64_e32 v[4:5], s[12:13]
	v_mov_b64_e32 v[6:7], s[14:15]
	v_mov_b64_e32 v[8:9], s[16:17]
	v_mov_b64_e32 v[10:11], s[18:19]
	v_mov_b64_e32 v[12:13], s[20:21]
	v_mov_b64_e32 v[14:15], s[22:23]
	s_nop 15
	s_nop 3
	v_cvt_pk_f16_f32 v239, v64, v65
	v_cvt_pk_f16_f32 v240, v66, v67
	v_and_b32 v209, s35, v239
	v_and_b32 v238, s35, v240
	v_pk_fma_f16 v236, v209, s42, v227
	v_pk_fma_f16 v237, v238, s42, v227
	v_pk_fma_f16 v236, v236, v209, s43
	v_pk_fma_f16 v237, v237, v238, s43
	v_pk_mul_f16 v236, v236, v209
	v_pk_mul_f16 v237, v237, v238
	v_exp_f16_sdwa v236, v236 dst_sel:WORD_0 dst_unused:UNUSED_PRESERVE src0_sel:WORD_0
	v_exp_f16_sdwa v237, v237 dst_sel:WORD_0 dst_unused:UNUSED_PRESERVE src0_sel:WORD_0
	v_exp_f16_sdwa v236, v236 dst_sel:WORD_1 dst_unused:UNUSED_PRESERVE src0_sel:WORD_1
	v_exp_f16_sdwa v237, v237 dst_sel:WORD_1 dst_unused:UNUSED_PRESERVE src0_sel:WORD_1
	v_pk_add_f16 v64, v239, v209
	v_pk_add_f16 v65, v240, v238
	v_pk_fma_f16 v236, v209, v236, v64 neg_lo:[1,0,0] neg_hi:[1,0,0]
	v_pk_fma_f16 v237, v238, v237, v65 neg_lo:[1,0,0] neg_hi:[1,0,0]
	v_cvt_pk_f16_f32 v209, v68, v69
	v_cvt_pk_f16_f32 v238, v70, v71
	v_and_b32 v66, s35, v209
	v_and_b32 v67, s35, v238
	v_pk_fma_f16 v64, v66, s42, v227
	v_pk_fma_f16 v65, v67, s42, v227
	v_pk_fma_f16 v64, v64, v66, s43
	v_pk_fma_f16 v65, v65, v67, s43
	v_pk_mul_f16 v64, v64, v66
	v_pk_mul_f16 v65, v65, v67
	v_exp_f16_sdwa v64, v64 dst_sel:WORD_0 dst_unused:UNUSED_PRESERVE src0_sel:WORD_0
	v_exp_f16_sdwa v65, v65 dst_sel:WORD_0 dst_unused:UNUSED_PRESERVE src0_sel:WORD_0
	v_exp_f16_sdwa v64, v64 dst_sel:WORD_1 dst_unused:UNUSED_PRESERVE src0_sel:WORD_1
	v_exp_f16_sdwa v65, v65 dst_sel:WORD_1 dst_unused:UNUSED_PRESERVE src0_sel:WORD_1
	v_pk_add_f16 v68, v209, v66
	v_pk_add_f16 v69, v238, v67
	v_pk_fma_f16 v64, v66, v64, v68 neg_lo:[1,0,0] neg_hi:[1,0,0]
	v_pk_fma_f16 v65, v67, v65, v69 neg_lo:[1,0,0] neg_hi:[1,0,0]
	v_cvt_pk_f16_f32 v70, v72, v73
	v_cvt_pk_f16_f32 v71, v74, v75
	v_and_b32 v68, s35, v70
	v_and_b32 v69, s35, v71
	v_pk_fma_f16 v66, v68, s42, v227
	v_pk_fma_f16 v67, v69, s42, v227
	v_pk_fma_f16 v66, v66, v68, s43
	v_pk_fma_f16 v67, v67, v69, s43
	v_pk_mul_f16 v66, v66, v68
	v_pk_mul_f16 v67, v67, v69
	v_exp_f16_sdwa v66, v66 dst_sel:WORD_0 dst_unused:UNUSED_PRESERVE src0_sel:WORD_0
	v_exp_f16_sdwa v67, v67 dst_sel:WORD_0 dst_unused:UNUSED_PRESERVE src0_sel:WORD_0
	v_exp_f16_sdwa v66, v66 dst_sel:WORD_1 dst_unused:UNUSED_PRESERVE src0_sel:WORD_1
	v_exp_f16_sdwa v67, v67 dst_sel:WORD_1 dst_unused:UNUSED_PRESERVE src0_sel:WORD_1
	v_pk_add_f16 v72, v70, v68
	v_pk_add_f16 v73, v71, v69
	v_pk_fma_f16 v66, v68, v66, v72 neg_lo:[1,0,0] neg_hi:[1,0,0]
	v_pk_fma_f16 v67, v69, v67, v73 neg_lo:[1,0,0] neg_hi:[1,0,0]
	v_cvt_pk_f16_f32 v72, v76, v77
	v_cvt_pk_f16_f32 v73, v78, v79
	v_and_b32 v70, s35, v72
	v_and_b32 v71, s35, v73
	v_pk_fma_f16 v68, v70, s42, v227
	v_pk_fma_f16 v69, v71, s42, v227
	v_pk_fma_f16 v68, v68, v70, s43
	v_pk_fma_f16 v69, v69, v71, s43
	v_pk_mul_f16 v68, v68, v70
	v_pk_mul_f16 v69, v69, v71
	v_exp_f16_sdwa v68, v68 dst_sel:WORD_0 dst_unused:UNUSED_PRESERVE src0_sel:WORD_0
	v_exp_f16_sdwa v69, v69 dst_sel:WORD_0 dst_unused:UNUSED_PRESERVE src0_sel:WORD_0
	v_exp_f16_sdwa v68, v68 dst_sel:WORD_1 dst_unused:UNUSED_PRESERVE src0_sel:WORD_1
	v_exp_f16_sdwa v69, v69 dst_sel:WORD_1 dst_unused:UNUSED_PRESERVE src0_sel:WORD_1
	v_pk_add_f16 v74, v72, v70
	v_pk_add_f16 v75, v73, v71
	v_pk_fma_f16 v68, v70, v68, v74 neg_lo:[1,0,0] neg_hi:[1,0,0]
	v_pk_fma_f16 v69, v71, v69, v75 neg_lo:[1,0,0] neg_hi:[1,0,0]
	v_cvt_pk_f16_f32 v74, v48, v49
	v_cvt_pk_f16_f32 v75, v50, v51
	v_and_b32 v72, s35, v74
	v_and_b32 v73, s35, v75
	v_pk_fma_f16 v70, v72, s42, v227
	v_pk_fma_f16 v71, v73, s42, v227
	v_pk_fma_f16 v70, v70, v72, s43
	v_pk_fma_f16 v71, v71, v73, s43
	v_pk_mul_f16 v70, v70, v72
	v_pk_mul_f16 v71, v71, v73
	v_exp_f16_sdwa v70, v70 dst_sel:WORD_0 dst_unused:UNUSED_PRESERVE src0_sel:WORD_0
	v_exp_f16_sdwa v71, v71 dst_sel:WORD_0 dst_unused:UNUSED_PRESERVE src0_sel:WORD_0
	v_exp_f16_sdwa v70, v70 dst_sel:WORD_1 dst_unused:UNUSED_PRESERVE src0_sel:WORD_1
	v_exp_f16_sdwa v71, v71 dst_sel:WORD_1 dst_unused:UNUSED_PRESERVE src0_sel:WORD_1
	v_pk_add_f16 v48, v74, v72
	v_pk_add_f16 v49, v75, v73
	v_pk_fma_f16 v70, v72, v70, v48 neg_lo:[1,0,0] neg_hi:[1,0,0]
	v_pk_fma_f16 v71, v73, v71, v49 neg_lo:[1,0,0] neg_hi:[1,0,0]
	v_cvt_pk_f16_f32 v72, v52, v53
	v_cvt_pk_f16_f32 v73, v54, v55
	v_and_b32 v50, s35, v72
	v_and_b32 v51, s35, v73
	v_pk_fma_f16 v48, v50, s42, v227
	v_pk_fma_f16 v49, v51, s42, v227
	v_pk_fma_f16 v48, v48, v50, s43
	v_pk_fma_f16 v49, v49, v51, s43
	v_pk_mul_f16 v48, v48, v50
	v_pk_mul_f16 v49, v49, v51
	v_exp_f16_sdwa v48, v48 dst_sel:WORD_0 dst_unused:UNUSED_PRESERVE src0_sel:WORD_0
	v_exp_f16_sdwa v49, v49 dst_sel:WORD_0 dst_unused:UNUSED_PRESERVE src0_sel:WORD_0
	v_exp_f16_sdwa v48, v48 dst_sel:WORD_1 dst_unused:UNUSED_PRESERVE src0_sel:WORD_1
	v_exp_f16_sdwa v49, v49 dst_sel:WORD_1 dst_unused:UNUSED_PRESERVE src0_sel:WORD_1
	v_pk_add_f16 v52, v72, v50
	v_pk_add_f16 v53, v73, v51
	v_pk_fma_f16 v48, v50, v48, v52 neg_lo:[1,0,0] neg_hi:[1,0,0]
	v_pk_fma_f16 v49, v51, v49, v53 neg_lo:[1,0,0] neg_hi:[1,0,0]
	v_cvt_pk_f16_f32 v54, v56, v57
	v_cvt_pk_f16_f32 v55, v58, v59
	v_and_b32 v52, s35, v54
	v_and_b32 v53, s35, v55
	v_pk_fma_f16 v50, v52, s42, v227
	v_pk_fma_f16 v51, v53, s42, v227
	v_pk_fma_f16 v50, v50, v52, s43
	v_pk_fma_f16 v51, v51, v53, s43
	v_pk_mul_f16 v50, v50, v52
	v_pk_mul_f16 v51, v51, v53
	v_exp_f16_sdwa v50, v50 dst_sel:WORD_0 dst_unused:UNUSED_PRESERVE src0_sel:WORD_0
	v_exp_f16_sdwa v51, v51 dst_sel:WORD_0 dst_unused:UNUSED_PRESERVE src0_sel:WORD_0
	v_exp_f16_sdwa v50, v50 dst_sel:WORD_1 dst_unused:UNUSED_PRESERVE src0_sel:WORD_1
	v_exp_f16_sdwa v51, v51 dst_sel:WORD_1 dst_unused:UNUSED_PRESERVE src0_sel:WORD_1
	v_pk_add_f16 v56, v54, v52
	v_pk_add_f16 v57, v55, v53
	v_pk_fma_f16 v50, v52, v50, v56 neg_lo:[1,0,0] neg_hi:[1,0,0]
	v_pk_fma_f16 v51, v53, v51, v57 neg_lo:[1,0,0] neg_hi:[1,0,0]
	v_cvt_pk_f16_f32 v56, v60, v61
	v_cvt_pk_f16_f32 v57, v62, v63
	v_and_b32 v54, s35, v56
	v_and_b32 v55, s35, v57
	v_pk_fma_f16 v52, v54, s42, v227
	v_pk_fma_f16 v53, v55, s42, v227
	v_pk_fma_f16 v52, v52, v54, s43
	v_pk_fma_f16 v53, v53, v55, s43
	v_pk_mul_f16 v52, v52, v54
	v_pk_mul_f16 v53, v53, v55
	v_exp_f16_sdwa v52, v52 dst_sel:WORD_0 dst_unused:UNUSED_PRESERVE src0_sel:WORD_0
	v_exp_f16_sdwa v53, v53 dst_sel:WORD_0 dst_unused:UNUSED_PRESERVE src0_sel:WORD_0
	v_exp_f16_sdwa v52, v52 dst_sel:WORD_1 dst_unused:UNUSED_PRESERVE src0_sel:WORD_1
	v_exp_f16_sdwa v53, v53 dst_sel:WORD_1 dst_unused:UNUSED_PRESERVE src0_sel:WORD_1
	v_pk_add_f16 v58, v56, v54
	v_pk_add_f16 v59, v57, v55
	v_pk_fma_f16 v52, v54, v52, v58 neg_lo:[1,0,0] neg_hi:[1,0,0]
	v_pk_fma_f16 v53, v55, v53, v59 neg_lo:[1,0,0] neg_hi:[1,0,0]
	ds_write2_b64 v228, v[236:237], v[70:71] offset0:78 offset1:142
	ds_write2st64_b64 v231, v[64:65], v[48:49] offset0:5 offset1:6
	ds_write2st64_b64 v232, v[66:67], v[50:51] offset0:9 offset1:10
	ds_write2st64_b64 v233, v[68:69], v[52:53] offset0:13 offset1:14
	v_cvt_pk_f16_f32 v52, v32, v33
	v_cvt_pk_f16_f32 v53, v34, v35
	v_and_b32 v50, s35, v52
	v_and_b32 v51, s35, v53
	v_pk_fma_f16 v48, v50, s42, v227
	v_pk_fma_f16 v49, v51, s42, v227
	v_pk_fma_f16 v48, v48, v50, s43
	v_pk_fma_f16 v49, v49, v51, s43
	v_mov_b32_e32 v237, 0xff800000
	v_pk_mul_f16 v48, v48, v50
	v_pk_mul_f16 v49, v49, v51
	v_exp_f16_sdwa v48, v48 dst_sel:WORD_0 dst_unused:UNUSED_PRESERVE src0_sel:WORD_0
	v_exp_f16_sdwa v49, v49 dst_sel:WORD_0 dst_unused:UNUSED_PRESERVE src0_sel:WORD_0
	v_exp_f16_sdwa v48, v48 dst_sel:WORD_1 dst_unused:UNUSED_PRESERVE src0_sel:WORD_1
	v_exp_f16_sdwa v49, v49 dst_sel:WORD_1 dst_unused:UNUSED_PRESERVE src0_sel:WORD_1
	v_pk_add_f16 v32, v52, v50
	v_pk_add_f16 v33, v53, v51
	v_pk_fma_f16 v48, v50, v48, v32 neg_lo:[1,0,0] neg_hi:[1,0,0]
	v_pk_fma_f16 v49, v51, v49, v33 neg_lo:[1,0,0] neg_hi:[1,0,0]
	v_mov_b32_e32 v236, 0
	v_cvt_pk_f16_f32 v50, v36, v37
	v_cvt_pk_f16_f32 v51, v38, v39
	v_and_b32 v34, s35, v50
	v_and_b32 v35, s35, v51
	v_pk_fma_f16 v32, v34, s42, v227
	v_pk_fma_f16 v33, v35, s42, v227
	v_pk_fma_f16 v32, v32, v34, s43
	v_pk_fma_f16 v33, v33, v35, s43
	v_pk_mul_f16 v32, v32, v34
	v_pk_mul_f16 v33, v33, v35
	v_exp_f16_sdwa v32, v32 dst_sel:WORD_0 dst_unused:UNUSED_PRESERVE src0_sel:WORD_0
	v_exp_f16_sdwa v33, v33 dst_sel:WORD_0 dst_unused:UNUSED_PRESERVE src0_sel:WORD_0
	v_exp_f16_sdwa v32, v32 dst_sel:WORD_1 dst_unused:UNUSED_PRESERVE src0_sel:WORD_1
	v_exp_f16_sdwa v33, v33 dst_sel:WORD_1 dst_unused:UNUSED_PRESERVE src0_sel:WORD_1
	v_pk_add_f16 v36, v50, v34
	v_pk_add_f16 v37, v51, v35
	v_pk_fma_f16 v32, v34, v32, v36 neg_lo:[1,0,0] neg_hi:[1,0,0]
	v_pk_fma_f16 v33, v35, v33, v37 neg_lo:[1,0,0] neg_hi:[1,0,0]
	v_cvt_pk_f16_f32 v38, v40, v41
	v_cvt_pk_f16_f32 v39, v42, v43
	v_and_b32 v36, s35, v38
	v_and_b32 v37, s35, v39
	v_pk_fma_f16 v34, v36, s42, v227
	v_pk_fma_f16 v35, v37, s42, v227
	v_pk_fma_f16 v34, v34, v36, s43
	v_pk_fma_f16 v35, v35, v37, s43
	v_pk_mul_f16 v34, v34, v36
	v_pk_mul_f16 v35, v35, v37
	v_exp_f16_sdwa v34, v34 dst_sel:WORD_0 dst_unused:UNUSED_PRESERVE src0_sel:WORD_0
	v_exp_f16_sdwa v35, v35 dst_sel:WORD_0 dst_unused:UNUSED_PRESERVE src0_sel:WORD_0
	v_exp_f16_sdwa v34, v34 dst_sel:WORD_1 dst_unused:UNUSED_PRESERVE src0_sel:WORD_1
	v_exp_f16_sdwa v35, v35 dst_sel:WORD_1 dst_unused:UNUSED_PRESERVE src0_sel:WORD_1
	v_pk_add_f16 v40, v38, v36
	v_pk_add_f16 v41, v39, v37
	v_pk_fma_f16 v34, v36, v34, v40 neg_lo:[1,0,0] neg_hi:[1,0,0]
	v_pk_fma_f16 v35, v37, v35, v41 neg_lo:[1,0,0] neg_hi:[1,0,0]
	v_cvt_pk_f16_f32 v40, v44, v45
	v_cvt_pk_f16_f32 v41, v46, v47
	v_and_b32 v38, s35, v40
	v_and_b32 v39, s35, v41
	v_pk_fma_f16 v36, v38, s42, v227
	v_pk_fma_f16 v37, v39, s42, v227
	v_pk_fma_f16 v36, v36, v38, s43
	v_pk_fma_f16 v37, v37, v39, s43
	v_pk_mul_f16 v36, v36, v38
	v_pk_mul_f16 v37, v37, v39
	v_exp_f16_sdwa v36, v36 dst_sel:WORD_0 dst_unused:UNUSED_PRESERVE src0_sel:WORD_0
	v_exp_f16_sdwa v37, v37 dst_sel:WORD_0 dst_unused:UNUSED_PRESERVE src0_sel:WORD_0
	v_exp_f16_sdwa v36, v36 dst_sel:WORD_1 dst_unused:UNUSED_PRESERVE src0_sel:WORD_1
	v_exp_f16_sdwa v37, v37 dst_sel:WORD_1 dst_unused:UNUSED_PRESERVE src0_sel:WORD_1
	v_pk_add_f16 v42, v40, v38
	v_pk_add_f16 v43, v41, v39
	v_pk_fma_f16 v36, v38, v36, v42 neg_lo:[1,0,0] neg_hi:[1,0,0]
	v_pk_fma_f16 v37, v39, v37, v43 neg_lo:[1,0,0] neg_hi:[1,0,0]
	v_cvt_pk_f16_f32 v42, v16, v17
	v_cvt_pk_f16_f32 v43, v18, v19
	v_and_b32 v40, s35, v42
	v_and_b32 v41, s35, v43
	v_pk_fma_f16 v38, v40, s42, v227
	v_pk_fma_f16 v39, v41, s42, v227
	v_pk_fma_f16 v38, v38, v40, s43
	v_pk_fma_f16 v39, v39, v41, s43
	v_pk_mul_f16 v38, v38, v40
	v_pk_mul_f16 v39, v39, v41
	v_exp_f16_sdwa v38, v38 dst_sel:WORD_0 dst_unused:UNUSED_PRESERVE src0_sel:WORD_0
	v_exp_f16_sdwa v39, v39 dst_sel:WORD_0 dst_unused:UNUSED_PRESERVE src0_sel:WORD_0
	v_exp_f16_sdwa v38, v38 dst_sel:WORD_1 dst_unused:UNUSED_PRESERVE src0_sel:WORD_1
	v_exp_f16_sdwa v39, v39 dst_sel:WORD_1 dst_unused:UNUSED_PRESERVE src0_sel:WORD_1
	v_pk_add_f16 v16, v42, v40
	v_pk_add_f16 v17, v43, v41
	v_pk_fma_f16 v38, v40, v38, v16 neg_lo:[1,0,0] neg_hi:[1,0,0]
	v_pk_fma_f16 v39, v41, v39, v17 neg_lo:[1,0,0] neg_hi:[1,0,0]
	v_cvt_pk_f16_f32 v40, v20, v21
	v_cvt_pk_f16_f32 v41, v22, v23
	v_and_b32 v18, s35, v40
	v_and_b32 v19, s35, v41
	v_pk_fma_f16 v16, v18, s42, v227
	v_pk_fma_f16 v17, v19, s42, v227
	v_pk_fma_f16 v16, v16, v18, s43
	v_pk_fma_f16 v17, v17, v19, s43
	v_pk_mul_f16 v16, v16, v18
	v_pk_mul_f16 v17, v17, v19
	v_exp_f16_sdwa v16, v16 dst_sel:WORD_0 dst_unused:UNUSED_PRESERVE src0_sel:WORD_0
	v_exp_f16_sdwa v17, v17 dst_sel:WORD_0 dst_unused:UNUSED_PRESERVE src0_sel:WORD_0
	v_exp_f16_sdwa v16, v16 dst_sel:WORD_1 dst_unused:UNUSED_PRESERVE src0_sel:WORD_1
	v_exp_f16_sdwa v17, v17 dst_sel:WORD_1 dst_unused:UNUSED_PRESERVE src0_sel:WORD_1
	v_pk_add_f16 v20, v40, v18
	v_pk_add_f16 v21, v41, v19
	v_pk_fma_f16 v16, v18, v16, v20 neg_lo:[1,0,0] neg_hi:[1,0,0]
	v_pk_fma_f16 v17, v19, v17, v21 neg_lo:[1,0,0] neg_hi:[1,0,0]
	v_cvt_pk_f16_f32 v22, v24, v25
	v_cvt_pk_f16_f32 v23, v26, v27
	v_and_b32 v20, s35, v22
	v_and_b32 v21, s35, v23
	v_pk_fma_f16 v18, v20, s42, v227
	v_pk_fma_f16 v19, v21, s42, v227
	v_pk_fma_f16 v18, v18, v20, s43
	v_pk_fma_f16 v19, v19, v21, s43
	v_pk_mul_f16 v18, v18, v20
	v_pk_mul_f16 v19, v19, v21
	v_exp_f16_sdwa v18, v18 dst_sel:WORD_0 dst_unused:UNUSED_PRESERVE src0_sel:WORD_0
	v_exp_f16_sdwa v19, v19 dst_sel:WORD_0 dst_unused:UNUSED_PRESERVE src0_sel:WORD_0
	v_exp_f16_sdwa v18, v18 dst_sel:WORD_1 dst_unused:UNUSED_PRESERVE src0_sel:WORD_1
	v_exp_f16_sdwa v19, v19 dst_sel:WORD_1 dst_unused:UNUSED_PRESERVE src0_sel:WORD_1
	v_pk_add_f16 v24, v22, v20
	v_pk_add_f16 v25, v23, v21
	v_pk_fma_f16 v18, v20, v18, v24 neg_lo:[1,0,0] neg_hi:[1,0,0]
	v_pk_fma_f16 v19, v21, v19, v25 neg_lo:[1,0,0] neg_hi:[1,0,0]
	v_cvt_pk_f16_f32 v24, v28, v29
	v_cvt_pk_f16_f32 v25, v30, v31
	v_and_b32 v22, s35, v24
	v_and_b32 v23, s35, v25
	v_pk_fma_f16 v20, v22, s42, v227
	v_pk_fma_f16 v21, v23, s42, v227
	v_pk_fma_f16 v20, v20, v22, s43
	v_pk_fma_f16 v21, v21, v23, s43
	v_pk_mul_f16 v20, v20, v22
	v_pk_mul_f16 v21, v21, v23
	v_exp_f16_sdwa v20, v20 dst_sel:WORD_0 dst_unused:UNUSED_PRESERVE src0_sel:WORD_0
	v_exp_f16_sdwa v21, v21 dst_sel:WORD_0 dst_unused:UNUSED_PRESERVE src0_sel:WORD_0
	v_exp_f16_sdwa v20, v20 dst_sel:WORD_1 dst_unused:UNUSED_PRESERVE src0_sel:WORD_1
	v_exp_f16_sdwa v21, v21 dst_sel:WORD_1 dst_unused:UNUSED_PRESERVE src0_sel:WORD_1
	v_pk_add_f16 v26, v24, v22
	v_pk_add_f16 v27, v25, v23
	v_pk_fma_f16 v20, v22, v20, v26 neg_lo:[1,0,0] neg_hi:[1,0,0]
	v_pk_fma_f16 v21, v23, v21, v27 neg_lo:[1,0,0] neg_hi:[1,0,0]
	ds_write2st64_b64 v234, v[48:49], v[38:39] offset0:3 offset1:4
	ds_write2st64_b64 v231, v[32:33], v[16:17] offset0:7 offset1:8
	ds_write2st64_b64 v232, v[34:35], v[18:19] offset0:11 offset1:12
	ds_write2st64_b64 v233, v[36:37], v[20:21] offset0:15 offset1:16
	s_mul_i32 s0, s3, 0x280
	v_add_u32_e32 v44, s0, v248
	ds_read_b128 v[16:19], v44
	ds_read_b128 v[20:23], v44 offset:64
	v_mov_b32_e32 v252, 0
	v_mov_b32_e32 v253, 0
	v_mov_b32_e32 v254, 0
	v_mov_b32_e32 v255, 0
	s_waitcnt vmcnt(2)
	s_branch .LBB0_25

.Lno_pre:
	s_nop 15
	s_nop 3
	v_cvt_pk_f16_f32 v38, v64, v65
	v_cvt_pk_f16_f32 v39, v66, v67
	v_and_b32 v36, s35, v38
	v_and_b32 v37, s35, v39
	v_pk_fma_f16 v238, v36, s42, v227
	v_pk_fma_f16 v239, v37, s42, v227
	v_pk_fma_f16 v238, v238, v36, s43
	v_pk_fma_f16 v239, v239, v37, s43
	v_pk_mul_f16 v238, v238, v36
	v_pk_mul_f16 v239, v239, v37
	v_exp_f16_sdwa v238, v238 dst_sel:WORD_0 dst_unused:UNUSED_PRESERVE src0_sel:WORD_0
	v_exp_f16_sdwa v239, v239 dst_sel:WORD_0 dst_unused:UNUSED_PRESERVE src0_sel:WORD_0
	v_exp_f16_sdwa v238, v238 dst_sel:WORD_1 dst_unused:UNUSED_PRESERVE src0_sel:WORD_1
	v_exp_f16_sdwa v239, v239 dst_sel:WORD_1 dst_unused:UNUSED_PRESERVE src0_sel:WORD_1
	v_pk_add_f16 v40, v38, v36
	v_pk_add_f16 v41, v39, v37
	v_pk_fma_f16 v238, v36, v238, v40 neg_lo:[1,0,0] neg_hi:[1,0,0]
	v_pk_fma_f16 v239, v37, v239, v41 neg_lo:[1,0,0] neg_hi:[1,0,0]
	v_cvt_pk_f16_f32 v38, v68, v69
	v_cvt_pk_f16_f32 v39, v70, v71
	v_and_b32 v36, s35, v38
	v_and_b32 v37, s35, v39
	v_pk_fma_f16 v240, v36, s42, v227
	v_pk_fma_f16 v241, v37, s42, v227
	v_pk_fma_f16 v240, v240, v36, s43
	v_pk_fma_f16 v241, v241, v37, s43
	v_cvt_pk_f16_f32 v243, v72, v73
	v_cvt_pk_f16_f32 v244, v74, v75
	v_and_b32 v209, s35, v243
	v_and_b32 v242, s35, v244
	v_pk_fma_f16 v68, v209, s42, v227
	v_pk_fma_f16 v69, v242, s42, v227
	v_pk_fma_f16 v68, v68, v209, s43
	v_pk_fma_f16 v69, v69, v242, s43
	v_cvt_pk_f16_f32 v74, v76, v77
	v_cvt_pk_f16_f32 v75, v78, v79
	v_and_b32 v72, s35, v74
	v_and_b32 v73, s35, v75
	v_pk_fma_f16 v70, v72, s42, v227
	v_pk_fma_f16 v71, v73, s42, v227
	v_pk_fma_f16 v70, v70, v72, s43
	v_pk_fma_f16 v71, v71, v73, s43
	s_cmp_eq_u32 s8, 0
	v_pk_mul_f16 v240, v240, v36
	v_pk_mul_f16 v241, v241, v37
	v_exp_f16_sdwa v240, v240 dst_sel:WORD_0 dst_unused:UNUSED_PRESERVE src0_sel:WORD_0
	v_exp_f16_sdwa v241, v241 dst_sel:WORD_0 dst_unused:UNUSED_PRESERVE src0_sel:WORD_0
	v_exp_f16_sdwa v240, v240 dst_sel:WORD_1 dst_unused:UNUSED_PRESERVE src0_sel:WORD_1
	v_exp_f16_sdwa v241, v241 dst_sel:WORD_1 dst_unused:UNUSED_PRESERVE src0_sel:WORD_1
	v_pk_add_f16 v40, v38, v36
	v_pk_add_f16 v41, v39, v37
	v_pk_fma_f16 v240, v36, v240, v40 neg_lo:[1,0,0] neg_hi:[1,0,0]
	v_pk_fma_f16 v241, v37, v241, v41 neg_lo:[1,0,0] neg_hi:[1,0,0]
	v_pk_mul_f16 v68, v68, v209
	v_pk_mul_f16 v69, v69, v242
	v_exp_f16_sdwa v68, v68 dst_sel:WORD_0 dst_unused:UNUSED_PRESERVE src0_sel:WORD_0
	v_exp_f16_sdwa v69, v69 dst_sel:WORD_0 dst_unused:UNUSED_PRESERVE src0_sel:WORD_0
	v_exp_f16_sdwa v68, v68 dst_sel:WORD_1 dst_unused:UNUSED_PRESERVE src0_sel:WORD_1
	v_exp_f16_sdwa v69, v69 dst_sel:WORD_1 dst_unused:UNUSED_PRESERVE src0_sel:WORD_1
	v_pk_add_f16 v76, v243, v209
	v_pk_add_f16 v77, v244, v242
	v_pk_fma_f16 v68, v209, v68, v76 neg_lo:[1,0,0] neg_hi:[1,0,0]
	v_pk_fma_f16 v69, v242, v69, v77 neg_lo:[1,0,0] neg_hi:[1,0,0]
	v_pk_mul_f16 v70, v70, v72
	v_pk_mul_f16 v71, v71, v73
	v_exp_f16_sdwa v70, v70 dst_sel:WORD_0 dst_unused:UNUSED_PRESERVE src0_sel:WORD_0
	v_exp_f16_sdwa v71, v71 dst_sel:WORD_0 dst_unused:UNUSED_PRESERVE src0_sel:WORD_0
	v_exp_f16_sdwa v70, v70 dst_sel:WORD_1 dst_unused:UNUSED_PRESERVE src0_sel:WORD_1
	v_exp_f16_sdwa v71, v71 dst_sel:WORD_1 dst_unused:UNUSED_PRESERVE src0_sel:WORD_1
	v_pk_add_f16 v76, v74, v72
	v_pk_add_f16 v77, v75, v73
	v_pk_fma_f16 v70, v72, v70, v76 neg_lo:[1,0,0] neg_hi:[1,0,0]
	v_pk_fma_f16 v71, v73, v71, v77 neg_lo:[1,0,0] neg_hi:[1,0,0]
	v_cvt_pk_f16_f32 v74, v48, v49
	v_cvt_pk_f16_f32 v75, v50, v51
	v_and_b32 v72, s35, v74
	v_and_b32 v73, s35, v75
	v_pk_fma_f16 v64, v72, s42, v227
	v_pk_fma_f16 v65, v73, s42, v227
	v_pk_fma_f16 v64, v64, v72, s43
	v_pk_fma_f16 v65, v65, v73, s43
	v_cvt_pk_f16_f32 v78, v52, v53
	v_cvt_pk_f16_f32 v79, v54, v55
	v_and_b32 v76, s35, v78
	v_and_b32 v77, s35, v79
	v_pk_fma_f16 v66, v76, s42, v227
	v_pk_fma_f16 v67, v77, s42, v227
	v_pk_fma_f16 v66, v66, v76, s43
	v_pk_fma_f16 v67, v67, v77, s43
	v_pk_mul_f16 v64, v64, v72
	v_pk_mul_f16 v65, v65, v73
	v_exp_f16_sdwa v64, v64 dst_sel:WORD_0 dst_unused:UNUSED_PRESERVE src0_sel:WORD_0
	v_exp_f16_sdwa v65, v65 dst_sel:WORD_0 dst_unused:UNUSED_PRESERVE src0_sel:WORD_0
	v_exp_f16_sdwa v64, v64 dst_sel:WORD_1 dst_unused:UNUSED_PRESERVE src0_sel:WORD_1
	v_exp_f16_sdwa v65, v65 dst_sel:WORD_1 dst_unused:UNUSED_PRESERVE src0_sel:WORD_1
	v_pk_add_f16 v209, v74, v72
	v_pk_add_f16 v242, v75, v73
	v_pk_fma_f16 v64, v72, v64, v209 neg_lo:[1,0,0] neg_hi:[1,0,0]
	v_pk_fma_f16 v65, v73, v65, v242 neg_lo:[1,0,0] neg_hi:[1,0,0]
	v_pk_mul_f16 v66, v66, v76
	v_pk_mul_f16 v67, v67, v77
	v_exp_f16_sdwa v66, v66 dst_sel:WORD_0 dst_unused:UNUSED_PRESERVE src0_sel:WORD_0
	v_exp_f16_sdwa v67, v67 dst_sel:WORD_0 dst_unused:UNUSED_PRESERVE src0_sel:WORD_0
	v_exp_f16_sdwa v66, v66 dst_sel:WORD_1 dst_unused:UNUSED_PRESERVE src0_sel:WORD_1
	v_exp_f16_sdwa v67, v67 dst_sel:WORD_1 dst_unused:UNUSED_PRESERVE src0_sel:WORD_1
	v_pk_add_f16 v72, v78, v76
	v_pk_add_f16 v73, v79, v77
	v_pk_fma_f16 v66, v76, v66, v72 neg_lo:[1,0,0] neg_hi:[1,0,0]
	v_pk_fma_f16 v67, v77, v67, v73 neg_lo:[1,0,0] neg_hi:[1,0,0]
	v_cvt_pk_f16_f32 v74, v56, v57
	v_cvt_pk_f16_f32 v75, v58, v59
	v_and_b32 v72, s35, v74
	v_and_b32 v73, s35, v75
	v_pk_fma_f16 v48, v72, s42, v227
	v_pk_fma_f16 v49, v73, s42, v227
	v_pk_fma_f16 v48, v48, v72, s43
	v_pk_fma_f16 v49, v49, v73, s43
	v_cvt_pk_f16_f32 v58, v60, v61
	v_cvt_pk_f16_f32 v59, v62, v63
	v_and_b32 v56, s35, v58
	v_and_b32 v57, s35, v59
	v_pk_fma_f16 v50, v56, s42, v227
	v_pk_fma_f16 v51, v57, s42, v227
	v_pk_fma_f16 v50, v50, v56, s43
	v_pk_fma_f16 v51, v51, v57, s43
	v_pk_mul_f16 v48, v48, v72
	v_pk_mul_f16 v49, v49, v73
	v_exp_f16_sdwa v48, v48 dst_sel:WORD_0 dst_unused:UNUSED_PRESERVE src0_sel:WORD_0
	v_exp_f16_sdwa v49, v49 dst_sel:WORD_0 dst_unused:UNUSED_PRESERVE src0_sel:WORD_0
	v_exp_f16_sdwa v48, v48 dst_sel:WORD_1 dst_unused:UNUSED_PRESERVE src0_sel:WORD_1
	v_exp_f16_sdwa v49, v49 dst_sel:WORD_1 dst_unused:UNUSED_PRESERVE src0_sel:WORD_1
	v_pk_add_f16 v62, v74, v72
	v_pk_add_f16 v63, v75, v73
	v_pk_fma_f16 v48, v72, v48, v62 neg_lo:[1,0,0] neg_hi:[1,0,0]
	v_pk_fma_f16 v49, v73, v49, v63 neg_lo:[1,0,0] neg_hi:[1,0,0]
	v_pk_mul_f16 v50, v50, v56
	v_pk_mul_f16 v51, v51, v57
	v_exp_f16_sdwa v50, v50 dst_sel:WORD_0 dst_unused:UNUSED_PRESERVE src0_sel:WORD_0
	v_exp_f16_sdwa v51, v51 dst_sel:WORD_0 dst_unused:UNUSED_PRESERVE src0_sel:WORD_0
	v_exp_f16_sdwa v50, v50 dst_sel:WORD_1 dst_unused:UNUSED_PRESERVE src0_sel:WORD_1
	v_exp_f16_sdwa v51, v51 dst_sel:WORD_1 dst_unused:UNUSED_PRESERVE src0_sel:WORD_1
	v_pk_add_f16 v62, v58, v56
	v_pk_add_f16 v63, v59, v57
	v_pk_fma_f16 v50, v56, v50, v62 neg_lo:[1,0,0] neg_hi:[1,0,0]
	v_pk_fma_f16 v51, v57, v51, v63 neg_lo:[1,0,0] neg_hi:[1,0,0]
	ds_write2_b64 v246, v[238:239], v[240:241] offset0:136 offset1:138
	ds_write2_b64 v246, v[64:65], v[66:67] offset0:144 offset1:146
	ds_write2_b64 v246, v[68:69], v[70:71] offset0:140 offset1:142
	ds_write2_b64 v246, v[48:49], v[50:51] offset0:148 offset1:150
	ds_read2_b64 v[24:27], v249 offset1:1
	ds_read2_b64 v[28:31], v249 offset0:8 offset1:9
	ds_read2_b64 v[40:43], v250 offset1:1
	ds_read2_b64 v[44:47], v250 offset0:8 offset1:9
	s_waitcnt lgkmcnt(2)
	v_mfma_f32_16x16x32_f16 v[32:35], v[24:27], v[16:19], v[252:255]
	v_mfma_f32_16x16x32_f16 v[32:35], v[28:31], v[20:23], v[32:35]
	s_waitcnt lgkmcnt(0)
	v_mfma_f32_16x16x32_f16 v[36:39], v[40:43], v[16:19], v[252:255]
	v_mfma_f32_16x16x32_f16 v[36:39], v[44:47], v[20:23], v[36:39]
	s_nop 7
	v_max3_f32 v52, v32, v33, v34
	v_max3_f32 v52, v52, v35, v36
	v_max3_f32 v52, v52, v37, v38
	v_max_f32_e32 v52, v52, v39
	v_mov_b32_e32 v53, v52
	s_nop 1
	v_permlane16_swap_b32_e32 v52, v53
	s_nop 0
	v_max_f32_e32 v52, v52, v53
	v_mov_b32_e32 v53, v52
	s_nop 1
	v_permlane32_swap_b32_e32 v52, v53
	s_nop 0
	v_max_f32_e32 v48, v52, v53
	s_cbranch_scc1 .LBB0_23
	v_cmp_lt_f32_e32 vcc, 0x41000000, v48
	s_cbranch_vccz .Lsm_nosub
	v_add_f32_e32 v237, v237, v48
	v_sub_f32_e32 v52, 0, v48
	v_exp_f32_e32 v52, v52
	v_sub_f32_e32 v252, 0, v237
	v_sub_f32_e32 v253, 0, v237
	v_sub_f32_e32 v254, 0, v237
	v_sub_f32_e32 v255, 0, v237
	v_pk_mul_f32 v[14:15], v[52:53], v[14:15] op_sel_hi:[0,1]
	v_pk_mul_f32 v[12:13], v[52:53], v[12:13] op_sel_hi:[0,1]
	v_pk_mul_f32 v[10:11], v[52:53], v[10:11] op_sel_hi:[0,1]
	v_pk_mul_f32 v[8:9], v[52:53], v[8:9] op_sel_hi:[0,1]
	v_pk_mul_f32 v[6:7], v[52:53], v[6:7] op_sel_hi:[0,1]
	v_pk_mul_f32 v[4:5], v[52:53], v[4:5] op_sel_hi:[0,1]
	v_pk_mul_f32 v[2:3], v[52:53], v[2:3] op_sel_hi:[0,1]
	v_pk_mul_f32 v[0:1], v[52:53], v[0:1] op_sel_hi:[0,1]
	v_mul_f32_e32 v236, v236, v52
	s_branch .LBB0_24
